# QKV K-loop: LDS-DMA refills issued 3 per MFMA phase between the MFMAs
# speedup vs baseline: 1.0418x; 1.0054x over previous
.LBB1_35:
	s_or_b64 exec, exec, s[16:17]
	s_cmp_lt_i32 s20, 16
	s_cselect_b64 s[16:17], -1, 0
	s_cmp_gt_i32 s20, 15
	v_bfe_u32 v9, v0, 6, 2
	s_cselect_b64 vcc, -1, 0
	v_cndmask_b32_e32 v83, v78, v9, vcc
	v_cndmask_b32_e32 v9, v9, v78, vcc
	s_and_b64 s[22:23], vcc, exec
	v_lshl_or_b32 v80, v9, 6, v42
	v_bfe_u32 v9, v0, 1, 3
	s_cselect_b32 s26, 0x2000, 0
	s_cselect_b32 s27, 0, 0x2000
	v_bitop3_b32 v9, v1, v9, 4 bitop3:0x36
	s_add_u32 s18, s24, s18
	v_lshlrev_b32_e32 v84, 4, v9
	v_add_lshl_u32 v8, v8, v3, 1
	v_mov_b32_e32 v9, v2
	s_addc_u32 s19, s25, s19
	v_lshl_add_u64 v[8:9], s[18:19], 0, v[8:9]
	s_mov_b64 s[22:23], 0x100
	v_lshl_add_u64 v[66:67], v[8:9], 0, s[22:23]
	v_add_lshl_u32 v8, v7, v3, 1
	v_mov_b32_e32 v9, v2
	v_lshl_add_u64 v[8:9], s[18:19], 0, v[8:9]
	v_add_lshl_u32 v6, v6, v3, 1
	v_mov_b32_e32 v7, v2
	v_lshl_add_u64 v[68:69], v[8:9], 0, s[22:23]
	v_lshl_add_u64 v[8:9], s[18:19], 0, v[6:7]
	v_or_b32_e32 v6, 0x80000, v6
	v_lshlrev_b32_e32 v82, 6, v83
	v_lshl_add_u64 v[6:7], s[18:19], 0, v[6:7]
	s_add_u32 s0, s0, s2
	v_or_b32_e32 v10, v82, v42
	v_lshl_add_u64 v[72:73], v[6:7], 0, s[22:23]
	v_add_lshl_u32 v6, v5, v3, 1
	v_mov_b32_e32 v7, v2
	s_addc_u32 s1, s1, s3
	v_add_lshl_u32 v4, v4, v3, 1
	v_mov_b32_e32 v5, v2
	v_lshlrev_b32_e32 v86, 7, v10
	v_bitop3_b32 v10, v43, v1, 7 bitop3:0x6c
	v_lshl_add_u64 v[6:7], s[0:1], 0, v[6:7]
	v_lshl_add_u64 v[4:5], s[0:1], 0, v[4:5]
	v_lshlrev_b32_e32 v85, 4, v10
	v_lshlrev_b32_e32 v81, 7, v80
	v_lshl_add_u64 v[70:71], v[8:9], 0, s[22:23]
	v_lshl_add_u64 v[74:75], v[6:7], 0, s[22:23]
	v_lshl_add_u64 v[76:77], v[4:5], 0, s[22:23]
	s_mov_b32 s18, 2
	s_mov_b64 s[0:1], 0
	s_lshl_b32 s3, s26, 1
	s_lshl_b32 s2, s27, 1
	v_mov_b32_e32 v3, v2
	v_mov_b32_e32 v4, v2
	v_mov_b32_e32 v5, v2
	v_mov_b32_e32 v6, v2
	v_mov_b32_e32 v7, v2
	v_mov_b32_e32 v8, v2
	v_mov_b32_e32 v9, v2
	v_mov_b32_e32 v10, v2
	v_mov_b32_e32 v11, v2
	v_mov_b32_e32 v12, v2
	v_mov_b32_e32 v13, v2
	v_mov_b32_e32 v14, v2
	v_mov_b32_e32 v15, v2
	v_mov_b32_e32 v16, v2
	v_mov_b32_e32 v17, v2
	v_mov_b32_e32 v18, v2
	v_mov_b32_e32 v19, v2
	v_mov_b32_e32 v20, v2
	v_mov_b32_e32 v21, v2
	v_mov_b32_e32 v22, v2
	v_mov_b32_e32 v23, v2
	v_mov_b32_e32 v24, v2
	v_mov_b32_e32 v25, v2
	v_mov_b32_e32 v26, v2
	v_mov_b32_e32 v27, v2
	v_mov_b32_e32 v28, v2
	v_mov_b32_e32 v29, v2
	v_mov_b32_e32 v30, v2
	v_mov_b32_e32 v31, v2
	v_mov_b32_e32 v32, v2
	v_mov_b32_e32 v33, v2
	v_mov_b32_e32 v34, v2
	v_mov_b32_e32 v35, v2
	v_mov_b32_e32 v36, v2
	v_mov_b32_e32 v37, v2
	v_mov_b32_e32 v38, v2
	v_mov_b32_e32 v39, v2
	v_mov_b32_e32 v40, v2
	v_mov_b32_e32 v41, v2
	v_mov_b32_e32 v42, v2
	v_mov_b32_e32 v43, v2
	v_mov_b32_e32 v44, v2
	v_mov_b32_e32 v45, v2
	v_mov_b32_e32 v46, v2
	v_mov_b32_e32 v47, v2
	v_mov_b32_e32 v48, v2
	v_mov_b32_e32 v49, v2
	v_mov_b32_e32 v50, v2
	v_mov_b32_e32 v51, v2
	v_mov_b32_e32 v52, v2
	v_mov_b32_e32 v53, v2
	v_mov_b32_e32 v54, v2
	v_mov_b32_e32 v55, v2
	v_mov_b32_e32 v56, v2
	v_mov_b32_e32 v57, v2
	v_mov_b32_e32 v58, v2
	v_mov_b32_e32 v59, v2
	v_mov_b32_e32 v60, v2
	v_mov_b32_e32 v61, v2
	v_mov_b32_e32 v62, v2
	v_mov_b32_e32 v63, v2
	v_mov_b32_e32 v64, v2
	v_mov_b32_e32 v65, v2
	v_readfirstlane_b32 s44, v79
.LBB1_36:
	s_mul_i32 s19, s7, 0xc000
	s_add_i32 s22, s19, s3
	s_add_i32 s19, s19, s2
	v_add_u32_e32 v87, s22, v86
	v_add_u32_e32 v122, s19, v81
	v_add_u32_e32 v100, v87, v85
	v_add_u32_e32 v116, v122, v85
	ds_read_b128 v[88:91], v100
	ds_read_b128 v[92:95], v100 offset:2048
	ds_read_b128 v[96:99], v100 offset:4096
	ds_read_b128 v[100:103], v100 offset:6144
	ds_read_b128 v[104:107], v116
	ds_read_b128 v[108:111], v116 offset:2048
	ds_read_b128 v[112:115], v116 offset:4096
	ds_read_b128 v[116:119], v116 offset:6144
	s_barrier
	s_mul_i32 s19, s18, 0xc000
	s_add_u32 s19, s19, s44
	s_setprio 1
	s_waitcnt lgkmcnt(0)
	v_mfma_f32_16x16x32_f16 v[62:65], v[88:91], v[104:107], v[62:65]
	v_mfma_f32_16x16x32_f16 v[58:61], v[88:91], v[108:111], v[58:61]
	v_mfma_f32_16x16x32_f16 v[54:57], v[88:91], v[112:115], v[54:57]
	v_mfma_f32_16x16x32_f16 v[50:53], v[88:91], v[116:119], v[50:53]
	s_mov_b32 m0, s19
	v_lshl_add_u64 v[120:121], v[76:77], 0, s[0:1]
	global_load_lds_dwordx4 v[120:121], off
	v_mfma_f32_16x16x32_f16 v[46:49], v[92:95], v[104:107], v[46:49]
	v_mfma_f32_16x16x32_f16 v[42:45], v[92:95], v[108:111], v[42:45]
	v_mfma_f32_16x16x32_f16 v[38:41], v[92:95], v[112:115], v[38:41]
	v_mfma_f32_16x16x32_f16 v[34:37], v[92:95], v[116:119], v[34:37]
	s_add_u32 m0, s19, 0x2000
	v_lshl_add_u64 v[120:121], v[74:75], 0, s[0:1]
	global_load_lds_dwordx4 v[120:121], off
	v_mfma_f32_16x16x32_f16 v[30:33], v[96:99], v[104:107], v[30:33]
	v_mfma_f32_16x16x32_f16 v[26:29], v[96:99], v[108:111], v[26:29]
	v_mfma_f32_16x16x32_f16 v[22:25], v[96:99], v[112:115], v[22:25]
	v_mfma_f32_16x16x32_f16 v[18:21], v[96:99], v[116:119], v[18:21]
	s_add_u32 m0, s19, 0x4000
	v_lshl_add_u64 v[120:121], v[70:71], 0, s[0:1]
	global_load_lds_dwordx4 v[120:121], off
	v_mfma_f32_16x16x32_f16 v[14:17], v[100:103], v[104:107], v[14:17]
	v_mfma_f32_16x16x32_f16 v[10:13], v[100:103], v[108:111], v[10:13]
	v_mfma_f32_16x16x32_f16 v[6:9], v[100:103], v[112:115], v[6:9]
	v_mfma_f32_16x16x32_f16 v[2:5], v[100:103], v[116:119], v[2:5]
	s_setprio 0
	s_barrier
	v_add_u32_e32 v87, v87, v84
	ds_read_b128 v[88:91], v87
	ds_read_b128 v[92:95], v87 offset:2048
	ds_read_b128 v[96:99], v87 offset:4096
	ds_read_b128 v[100:103], v87 offset:6144
	v_add_u32_e32 v87, v122, v84
	ds_read_b128 v[104:107], v87
	ds_read_b128 v[108:111], v87 offset:2048
	ds_read_b128 v[112:115], v87 offset:4096
	ds_read_b128 v[116:119], v87 offset:6144
	s_waitcnt vmcnt(3)
	s_barrier
	s_setprio 1
	s_waitcnt lgkmcnt(0)
	v_mfma_f32_16x16x32_f16 v[62:65], v[88:91], v[104:107], v[62:65]
	v_mfma_f32_16x16x32_f16 v[58:61], v[88:91], v[108:111], v[58:61]
	v_mfma_f32_16x16x32_f16 v[54:57], v[88:91], v[112:115], v[54:57]
	v_mfma_f32_16x16x32_f16 v[50:53], v[88:91], v[116:119], v[50:53]
	s_add_u32 m0, s19, 0x6000
	v_lshl_add_u64 v[120:121], v[68:69], 0, s[0:1]
	global_load_lds_dwordx4 v[120:121], off
	v_mfma_f32_16x16x32_f16 v[46:49], v[92:95], v[104:107], v[46:49]
	v_mfma_f32_16x16x32_f16 v[42:45], v[92:95], v[108:111], v[42:45]
	v_mfma_f32_16x16x32_f16 v[38:41], v[92:95], v[112:115], v[38:41]
	v_mfma_f32_16x16x32_f16 v[34:37], v[92:95], v[116:119], v[34:37]
	s_add_u32 m0, s19, 0x8000
	v_lshl_add_u64 v[120:121], v[72:73], 0, s[0:1]
	global_load_lds_dwordx4 v[120:121], off
	v_mfma_f32_16x16x32_f16 v[30:33], v[96:99], v[104:107], v[30:33]
	v_mfma_f32_16x16x32_f16 v[26:29], v[96:99], v[108:111], v[26:29]
	v_mfma_f32_16x16x32_f16 v[22:25], v[96:99], v[112:115], v[22:25]
	v_mfma_f32_16x16x32_f16 v[18:21], v[96:99], v[116:119], v[18:21]
	s_add_u32 m0, s19, 0xa000
	v_lshl_add_u64 v[120:121], v[66:67], 0, s[0:1]
	global_load_lds_dwordx4 v[120:121], off
	v_mfma_f32_16x16x32_f16 v[14:17], v[100:103], v[104:107], v[14:17]
	v_mfma_f32_16x16x32_f16 v[10:13], v[100:103], v[108:111], v[10:13]
	v_mfma_f32_16x16x32_f16 v[6:9], v[100:103], v[112:115], v[6:9]
	v_mfma_f32_16x16x32_f16 v[2:5], v[100:103], v[116:119], v[2:5]
	s_setprio 0
	s_barrier
	s_add_i32 s19, s7, 1
	s_cmp_lg_u32 s7, 2
	s_cselect_b32 s7, s19, 0
	s_add_i32 s19, s18, 1
	s_cmp_lg_u32 s18, 2
	s_cselect_b32 s18, s19, 0
	s_add_u32 s0, s0, 0x80
	s_addc_u32 s1, s1, 0
	s_cmpk_eq_i32 s0, 0x700
	s_cbranch_scc0 .LBB1_36
	s_mul_i32 s0, s7, 0xc000
	s_add_i32 s1, s0, s3
	v_add_u32_e32 v79, s1, v86
	v_add_u32_e32 v87, v79, v85
	s_add_i32 s0, s0, s2
	ds_read_b128 v[66:69], v87
	ds_read_b128 v[70:73], v87 offset:2048
	ds_read_b128 v[74:77], v87 offset:4096
	ds_read_b128 v[88:91], v87 offset:6144
	v_add_u32_e32 v87, s0, v81
	v_add_u32_e32 v104, v87, v85
	ds_read_b128 v[92:95], v104
	ds_read_b128 v[96:99], v104 offset:2048
	ds_read_b128 v[100:103], v104 offset:4096
	ds_read_b128 v[104:107], v104 offset:6144
	s_barrier
	s_setprio 1
	s_waitcnt lgkmcnt(0)
	v_mfma_f32_16x16x32_f16 v[62:65], v[66:69], v[92:95], v[62:65]
	v_mfma_f32_16x16x32_f16 v[58:61], v[66:69], v[96:99], v[58:61]
	v_mfma_f32_16x16x32_f16 v[54:57], v[66:69], v[100:103], v[54:57]
	v_mfma_f32_16x16x32_f16 v[50:53], v[66:69], v[104:107], v[50:53]
	v_mfma_f32_16x16x32_f16 v[46:49], v[70:73], v[92:95], v[46:49]
	v_mfma_f32_16x16x32_f16 v[42:45], v[70:73], v[96:99], v[42:45]
	v_mfma_f32_16x16x32_f16 v[38:41], v[70:73], v[100:103], v[38:41]
	v_mfma_f32_16x16x32_f16 v[34:37], v[70:73], v[104:107], v[34:37]
	v_mfma_f32_16x16x32_f16 v[30:33], v[74:77], v[92:95], v[30:33]
	v_mfma_f32_16x16x32_f16 v[26:29], v[74:77], v[96:99], v[26:29]
	v_mfma_f32_16x16x32_f16 v[22:25], v[74:77], v[100:103], v[22:25]
	v_mfma_f32_16x16x32_f16 v[18:21], v[74:77], v[104:107], v[18:21]
	v_mfma_f32_16x16x32_f16 v[14:17], v[88:91], v[92:95], v[14:17]
	v_mfma_f32_16x16x32_f16 v[10:13], v[88:91], v[96:99], v[10:13]
	v_mfma_f32_16x16x32_f16 v[6:9], v[88:91], v[100:103], v[6:9]
	v_mfma_f32_16x16x32_f16 v[2:5], v[88:91], v[104:107], v[2:5]
	s_setprio 0
	s_barrier
	v_add_u32_e32 v79, v79, v84
	ds_read_b128 v[66:69], v79
	ds_read_b128 v[70:73], v79 offset:2048
	ds_read_b128 v[74:77], v79 offset:4096
	ds_read_b128 v[88:91], v79 offset:6144
	v_add_u32_e32 v79, v87, v84
	ds_read_b128 v[92:95], v79
	ds_read_b128 v[96:99], v79 offset:2048
	ds_read_b128 v[100:103], v79 offset:4096
	ds_read_b128 v[104:107], v79 offset:6144
	s_waitcnt vmcnt(0)
	s_barrier
	s_setprio 1
	s_waitcnt lgkmcnt(0)
	v_mfma_f32_16x16x32_f16 v[62:65], v[66:69], v[92:95], v[62:65]
	v_mfma_f32_16x16x32_f16 v[58:61], v[66:69], v[96:99], v[58:61]
	v_mfma_f32_16x16x32_f16 v[54:57], v[66:69], v[100:103], v[54:57]
	v_mfma_f32_16x16x32_f16 v[50:53], v[66:69], v[104:107], v[50:53]
	v_mfma_f32_16x16x32_f16 v[46:49], v[70:73], v[92:95], v[46:49]
	v_mfma_f32_16x16x32_f16 v[42:45], v[70:73], v[96:99], v[42:45]
	v_mfma_f32_16x16x32_f16 v[38:41], v[70:73], v[100:103], v[38:41]
	v_mfma_f32_16x16x32_f16 v[34:37], v[70:73], v[104:107], v[34:37]
	v_mfma_f32_16x16x32_f16 v[30:33], v[74:77], v[92:95], v[30:33]
	v_mfma_f32_16x16x32_f16 v[26:29], v[74:77], v[96:99], v[26:29]
	v_mfma_f32_16x16x32_f16 v[22:25], v[74:77], v[100:103], v[22:25]
	v_mfma_f32_16x16x32_f16 v[18:21], v[74:77], v[104:107], v[18:21]
	v_mfma_f32_16x16x32_f16 v[14:17], v[88:91], v[92:95], v[14:17]
	v_mfma_f32_16x16x32_f16 v[10:13], v[88:91], v[96:99], v[10:13]
	v_mfma_f32_16x16x32_f16 v[6:9], v[88:91], v[100:103], v[6:9]
	v_mfma_f32_16x16x32_f16 v[2:5], v[88:91], v[104:107], v[2:5]
	s_setprio 0
	s_barrier
	v_add_u32_e32 v79, s3, v86
	v_add_u32_e32 v106, s2, v81
	v_add_u32_e32 v86, v79, v85
	v_add_u32_e32 v85, v106, v85
	ds_read_b128 v[66:69], v86
	ds_read_b128 v[70:73], v86 offset:2048
	ds_read_b128 v[74:77], v86 offset:4096
	ds_read_b128 v[86:89], v86 offset:6144
	ds_read_b128 v[90:93], v85
	ds_read_b128 v[94:97], v85 offset:2048
	ds_read_b128 v[98:101], v85 offset:4096
	ds_read_b128 v[102:105], v85 offset:6144
	s_barrier
	s_setprio 1
	s_waitcnt lgkmcnt(0)
	v_mfma_f32_16x16x32_f16 v[62:65], v[66:69], v[90:93], v[62:65]
	v_mfma_f32_16x16x32_f16 v[58:61], v[66:69], v[94:97], v[58:61]
	v_mfma_f32_16x16x32_f16 v[54:57], v[66:69], v[98:101], v[54:57]
	v_mfma_f32_16x16x32_f16 v[50:53], v[66:69], v[102:105], v[50:53]
	v_mfma_f32_16x16x32_f16 v[46:49], v[70:73], v[90:93], v[46:49]
	v_mfma_f32_16x16x32_f16 v[42:45], v[70:73], v[94:97], v[42:45]
	v_mfma_f32_16x16x32_f16 v[38:41], v[70:73], v[98:101], v[38:41]
	v_mfma_f32_16x16x32_f16 v[34:37], v[70:73], v[102:105], v[34:37]
	v_mfma_f32_16x16x32_f16 v[30:33], v[74:77], v[90:93], v[30:33]
	v_mfma_f32_16x16x32_f16 v[26:29], v[74:77], v[94:97], v[26:29]
	v_mfma_f32_16x16x32_f16 v[22:25], v[74:77], v[98:101], v[22:25]
	v_mfma_f32_16x16x32_f16 v[18:21], v[74:77], v[102:105], v[18:21]
	v_mfma_f32_16x16x32_f16 v[14:17], v[86:89], v[90:93], v[14:17]
	v_mfma_f32_16x16x32_f16 v[10:13], v[86:89], v[94:97], v[10:13]
	v_mfma_f32_16x16x32_f16 v[6:9], v[86:89], v[98:101], v[6:9]
	v_mfma_f32_16x16x32_f16 v[2:5], v[86:89], v[102:105], v[2:5]
	s_setprio 0
	s_barrier
	v_add_u32_e32 v85, v106, v84
	v_add_u32_e32 v79, v79, v84
	ds_read_b128 v[66:69], v85 offset:6144
	ds_read_b128 v[70:73], v85 offset:4096
	ds_read_b128 v[74:77], v85 offset:2048
	ds_read_b128 v[86:89], v85
	ds_read_b128 v[90:93], v79 offset:6144
	ds_read_b128 v[94:97], v79 offset:4096
	ds_read_b128 v[98:101], v79 offset:2048
	ds_read_b128 v[102:105], v79
	s_barrier
	s_setprio 1
	s_waitcnt lgkmcnt(0)
	v_mfma_f32_16x16x32_f16 v[62:65], v[102:105], v[86:89], v[62:65]
	v_mfma_f32_16x16x32_f16 v[58:61], v[102:105], v[74:77], v[58:61]
	v_mfma_f32_16x16x32_f16 v[54:57], v[102:105], v[70:73], v[54:57]
	v_mfma_f32_16x16x32_f16 v[50:53], v[102:105], v[66:69], v[50:53]
	v_mfma_f32_16x16x32_f16 v[46:49], v[98:101], v[86:89], v[46:49]
	v_mfma_f32_16x16x32_f16 v[42:45], v[98:101], v[74:77], v[42:45]
	v_mfma_f32_16x16x32_f16 v[38:41], v[98:101], v[70:73], v[38:41]
	v_mfma_f32_16x16x32_f16 v[34:37], v[98:101], v[66:69], v[34:37]
	v_mfma_f32_16x16x32_f16 v[30:33], v[94:97], v[86:89], v[30:33]
	v_mfma_f32_16x16x32_f16 v[26:29], v[94:97], v[74:77], v[26:29]
	v_mfma_f32_16x16x32_f16 v[22:25], v[94:97], v[70:73], v[22:25]
	v_mfma_f32_16x16x32_f16 v[18:21], v[94:97], v[66:69], v[18:21]
	v_mfma_f32_16x16x32_f16 v[14:17], v[90:93], v[86:89], v[14:17]
	v_mfma_f32_16x16x32_f16 v[10:13], v[90:93], v[74:77], v[10:13]
	v_mfma_f32_16x16x32_f16 v[6:9], v[90:93], v[70:73], v[6:9]
	v_mfma_f32_16x16x32_f16 v[2:5], v[90:93], v[66:69], v[2:5]
	s_setprio 0
	s_barrier
	s_movk_i32 s0, 0x100
	v_cmp_gt_u32_e32 vcc, s0, v0
	s_and_saveexec_b64 s[0:1], vcc
	s_cbranch_execz .LBB1_39
	s_barrier

amdhsa.kernels:
  - .agpr_count:     0
    .args:
      - .actual_access:  read_only
        .address_space:  global
        .offset:         0
        .size:           8
        .value_kind:     global_buffer
      - .actual_access:  read_only
        .address_space:  global
        .offset:         8
        .size:           8
        .value_kind:     global_buffer
      - .actual_access:  read_only
        .address_space:  global
        .offset:         16
        .size:           8
        .value_kind:     global_buffer
      - .actual_access:  read_only
        .address_space:  global
        .offset:         24
        .size:           8
        .value_kind:     global_buffer
      - .actual_access:  read_only
        .address_space:  global
        .offset:         32
        .size:           8
        .value_kind:     global_buffer
      - .actual_access:  read_only
        .address_space:  global
        .offset:         40
        .size:           8
        .value_kind:     global_buffer
      - .actual_access:  read_only
        .address_space:  global
        .offset:         48
        .size:           8
        .value_kind:     global_buffer
      - .address_space:  global
        .offset:         56
        .size:           8
        .value_kind:     global_buffer
      - .address_space:  global
        .offset:         64
        .size:           8
        .value_kind:     global_buffer
      - .actual_access:  read_only
        .address_space:  global
        .offset:         72
        .size:           8
        .value_kind:     global_buffer
      - .address_space:  global
        .offset:         80
        .size:           8
        .value_kind:     global_buffer
    .group_segment_fixed_size: 0
    .kernarg_segment_align: 8
    .kernarg_segment_size: 88
    .language:       OpenCL C
    .language_version:
      - 2
      - 0
    .max_flat_workgroup_size: 256
    .name:           _Z11prep_kernelPKfS0_S0_S0_S0_S0_S0_PDF16_S1_S1_S1_
    .private_segment_fixed_size: 0
    .sgpr_count:     23
    .sgpr_spill_count: 0
    .symbol:         _Z11prep_kernelPKfS0_S0_S0_S0_S0_S0_PDF16_S1_S1_S1_.kd
    .uniform_work_group_size: 1
    .uses_dynamic_stack: false
    .vgpr_count:     28
    .vgpr_spill_count: 0
    .wavefront_size: 64
  - .agpr_count:     0
    .args:
      - .offset:         0
        .size:           88
        .value_kind:     by_value
    .group_segment_fixed_size: 163840
    .kernarg_segment_align: 8
    .kernarg_segment_size: 88
    .language:       OpenCL C
    .language_version:
      - 2
      - 0
    .max_flat_workgroup_size: 512
    .name:           _Z12gemm1_kernel6G1Args
    .private_segment_fixed_size: 0
    .sgpr_count:     52
    .sgpr_spill_count: 0
    .symbol:         _Z12gemm1_kernel6G1Args.kd
    .uniform_work_group_size: 1
    .uses_dynamic_stack: false
    .vgpr_count:     144
    .vgpr_spill_count: 0
    .wavefront_size: 64
  - .agpr_count:     0
    .args:
      - .address_space:  global
        .offset:         0
        .size:           8
        .value_kind:     global_buffer
      - .address_space:  global
        .offset:         8
        .size:           8
        .value_kind:     global_buffer
      - .address_space:  global
        .offset:         16
        .size:           8
        .value_kind:     global_buffer
      - .actual_access:  read_only
        .address_space:  global
        .offset:         24
        .size:           8
        .value_kind:     global_buffer
      - .actual_access:  read_only
        .address_space:  global
        .offset:         32
        .size:           8
        .value_kind:     global_buffer
      - .actual_access:  read_only
        .address_space:  global
        .offset:         40
        .size:           8
        .value_kind:     global_buffer
      - .address_space:  global
        .offset:         48
        .size:           8
        .value_kind:     global_buffer
      - .actual_access:  read_only
        .address_space:  global
        .offset:         56
        .size:           8
        .value_kind:     global_buffer
      - .address_space:  global
        .offset:         64
        .size:           8
        .value_kind:     global_buffer
      - .actual_access:  read_only
        .address_space:  global
        .offset:         72
        .size:           8
        .value_kind:     global_buffer
      - .address_space:  global
        .offset:         80
        .size:           8
        .value_kind:     global_buffer
    .group_segment_fixed_size: 81920
    .kernarg_segment_align: 8
    .kernarg_segment_size: 88
    .language:       OpenCL C
    .language_version:
      - 2
      - 0
    .max_flat_workgroup_size: 512
    .name:           _Z11attn_kernelPKDF16_S0_S0_PKfS2_S2_S0_S2_PDF16_S2_S3_
    .private_segment_fixed_size: 0
    .sgpr_count:     62
    .sgpr_spill_count: 0
    .symbol:         _Z11attn_kernelPKDF16_S0_S0_PKfS2_S2_S0_S2_PDF16_S2_S3_.kd
    .uniform_work_group_size: 1
    .uses_dynamic_stack: false
    .vgpr_count:     126
    .vgpr_spill_count: 0
    .wavefront_size: 64
  - .agpr_count:     0
    .args:
      - .address_space:  global
        .offset:         0
        .size:           8
        .value_kind:     global_buffer
      - .address_space:  global
        .offset:         8
        .size:           8
        .value_kind:     global_buffer
      - .actual_access:  read_only
        .address_space:  global
        .offset:         16
        .size:           8
        .value_kind:     global_buffer
      - .actual_access:  write_only
        .address_space:  global
        .offset:         24
        .size:           8
        .value_kind:     global_buffer
    .group_segment_fixed_size: 122880
    .kernarg_segment_align: 8
    .kernarg_segment_size: 32
    .language:       OpenCL C
    .language_version:
      - 2
      - 0
    .max_flat_workgroup_size: 512
    .name:           _Z14outproj_kernelPKDF16_S0_PKfPf
    .private_segment_fixed_size: 0
    .sgpr_count:     30
    .sgpr_spill_count: 0
    .symbol:         _Z14outproj_kernelPKDF16_S0_PKfPf.kd
    .uniform_work_group_size: 1
    .uses_dynamic_stack: false
    .vgpr_count:     90
    .vgpr_spill_count: 0
    .wavefront_size: 64
